# speedup vs baseline: 1.0111x; 1.0078x over previous
.LBB2_440:
	s_or_b64 exec, exec, s[6:7]
	v_mov_b32_e32 v0, 0
	s_waitcnt lgkmcnt(0)
	s_barrier
	ds_read_b128 v[2:5], v0 offset:6720
	s_lshl_b64 s[14:15], s[10:11], 2
	s_add_u32 s14, s8, s14
	s_addc_u32 s15, s9, s15
	s_mov_b32 s16, 0x3e800000
	s_waitcnt lgkmcnt(0)
	v_readfirstlane_b32 s0, v2
	v_readfirstlane_b32 s2, v3
	v_readfirstlane_b32 s4, v4
	v_readfirstlane_b32 s6, v5
	s_lshl_b32 s0, s0, 12
	s_lshl_b32 s2, s2, 12
	s_lshl_b32 s4, s4, 12
	s_lshl_b32 s6, s6, 12
	s_add_u32 s0, s12, s0
	s_addc_u32 s1, s13, 0
	s_add_u32 s2, s12, s2
	s_addc_u32 s3, s13, 0
	s_add_u32 s4, s12, s4
	s_addc_u32 s5, s13, 0
	s_add_u32 s6, s12, s6
	s_addc_u32 s7, s13, 0
	global_load_dwordx4 v[6:9], v1, s[0:1] nt
	global_load_dwordx4 v[10:13], v1, s[2:3] nt
	global_load_dwordx4 v[18:21], v1, s[4:5] nt
	global_load_dwordx4 v[14:17], v1, s[6:7] nt
	s_waitcnt vmcnt(2)
	v_pk_add_f32 v[8:9], v[8:9], v[12:13]
	v_pk_add_f32 v[6:7], v[6:7], v[10:11]
	s_waitcnt vmcnt(1)
	v_pk_add_f32 v[4:5], v[8:9], v[20:21]
	v_pk_add_f32 v[2:3], v[6:7], v[18:19]
	s_waitcnt vmcnt(0)
	v_pk_add_f32 v[4:5], v[4:5], v[16:17]
	v_pk_add_f32 v[2:3], v[2:3], v[14:15]
	v_pk_mul_f32 v[4:5], v[4:5], s[16:17] op_sel_hi:[1,0]
	v_pk_mul_f32 v[2:3], v[2:3], s[16:17] op_sel_hi:[1,0]
	global_store_dwordx4 v1, v[2:5], s[14:15] nt
	s_endpgm
